# baseline (speedup 1.0000x reference)
.Lp4_last:
	s_lshl_b32 s48, s17, 18
	s_or_b32 s49, s49, s48
	s_mov_b32 m0, s28
	s_lshl_b32 s49, s49, 1
	ds_read_b128 v[162:165], v226 offset:49152
	ds_read_b128 v[166:169], v226 offset:51200
	ds_read_b128 v[170:173], v227 offset:49152
	ds_read_b128 v[174:177], v227 offset:51200
	ds_read_b128 v[178:181], v226 offset:53248
	ds_read_b128 v[182:185], v226 offset:55296
	ds_read_b128 v[186:189], v227 offset:53248
	ds_read_b128 v[190:193], v227 offset:55296
	buffer_load_dwordx4 v199, s[8:11], s49 offen lds
	s_mov_b32 m0, s29
	s_or_b32 s48, s51, s48
	buffer_load_dwordx4 v205, s[8:11], s49 offen lds
	s_lshl_b32 s48, s48, 1
	s_mov_b32 m0, s30
	s_lshl_b32 s17, s17, 22
	buffer_load_dwordx4 v199, s[8:11], s48 offen lds
	s_mov_b32 m0, s31
	s_add_i32 s17, s17, s47
	buffer_load_dwordx4 v205, s[8:11], s48 offen lds
	s_mov_b32 m0, s33
	s_nop 0
	buffer_load_dwordx4 v1, s[4:7], s17 offen lds
	s_mov_b32 m0, s34
	s_nop 0
	buffer_load_dwordx4 v204, s[4:7], s17 offen lds
	s_waitcnt lgkmcnt(0)
	s_waitcnt vmcnt(8)
	s_barrier
	s_setprio 1
	s_waitcnt lgkmcnt(0)
	v_mfma_f32_16x16x32_bf16 v[90:93], v[162:165], v[130:133], v[90:93]
	s_lshl_b32 s58, s42, 7
	v_mfma_f32_16x16x32_bf16 v[86:89], v[162:165], v[138:141], v[86:89]
	v_exp_f32_e32 v244, v114
	s_add_i32 s59, s41, 0x400
	v_mfma_f32_16x16x32_bf16 v[42:45], v[166:169], v[130:133], v[42:45]
	v_exp_f32_e32 v245, v115
	s_lshr_b32 s59, s59, 6
	v_mfma_f32_16x16x32_bf16 v[38:41], v[166:169], v[138:141], v[38:41]
	v_exp_f32_e32 v246, v116
	s_bfe_u32 s60, s20, 0x1000c
	v_mfma_f32_16x16x32_bf16 v[126:129], v[178:181], v[130:133], v[126:129]
	v_exp_f32_e32 v247, v117
	s_add_i32 s59, s59, s60
	v_mfma_f32_16x16x32_bf16 v[122:125], v[178:181], v[138:141], v[122:125]
	v_exp_f32_e32 v248, v78
	s_lshl_b32 s59, s59, 19
	v_mfma_f32_16x16x32_bf16 v[58:61], v[182:185], v[130:133], v[58:61]
	v_exp_f32_e32 v249, v79
	s_add_u32 s58, s58, s59
	v_mfma_f32_16x16x32_bf16 v[50:53], v[182:185], v[138:141], v[50:53]
	v_exp_f32_e32 v250, v80
	s_add_u32 s58, s56, s58
	v_mfma_f32_16x16x32_bf16 v[90:93], v[170:173], v[134:137], v[90:93]
	v_exp_f32_e32 v251, v81
	s_addc_u32 s59, s57, 0
	v_mfma_f32_16x16x32_bf16 v[86:89], v[170:173], v[142:145], v[86:89]
	v_exp_f32_e32 v252, v106
	s_add_u32 s60, s58, 0x4000
	v_mfma_f32_16x16x32_bf16 v[42:45], v[174:177], v[134:137], v[42:45]
	v_exp_f32_e32 v253, v107
	s_addc_u32 s61, s59, 0
	v_mfma_f32_16x16x32_bf16 v[38:41], v[174:177], v[142:145], v[38:41]
	v_exp_f32_e32 v254, v108
	s_add_u32 s62, s58, 0x100000
	v_mfma_f32_16x16x32_bf16 v[126:129], v[186:189], v[134:137], v[126:129]
	v_exp_f32_e32 v255, v109
	s_addc_u32 s63, s59, 0
	v_mfma_f32_16x16x32_bf16 v[122:125], v[186:189], v[142:145], v[122:125]
	v_exp_f32_e32 v232, v70
	s_add_u32 s64, s62, 0x4000
	v_mfma_f32_16x16x32_bf16 v[58:61], v[190:193], v[134:137], v[58:61]
	v_exp_f32_e32 v233, v71
	s_addc_u32 s65, s63, 0
	v_mfma_f32_16x16x32_bf16 v[50:53], v[190:193], v[142:145], v[50:53]
	v_exp_f32_e32 v234, v72
	s_lshr_b32 s66, s41, 7
	s_setprio 0
	s_setprio 1
	v_mfma_f32_16x16x32_bf16 v[82:85], v[162:165], v[146:149], v[82:85]
	v_exp_f32_e32 v235, v73
	s_bfe_u32 s67, s20, 0x1000c
	v_mfma_f32_16x16x32_bf16 v[22:25], v[162:165], v[154:157], v[22:25]
	s_add_i32 s66, s66, s67
	v_mfma_f32_16x16x32_bf16 v[34:37], v[166:169], v[146:149], v[34:37]
	s_lshl_b32 s66, s66, 14
	v_mfma_f32_16x16x32_bf16 v[6:9], v[166:169], v[154:157], v[6:9]
	s_lshl_b32 s67, s42, 2
	v_mfma_f32_16x16x32_bf16 v[118:121], v[178:181], v[146:149], v[118:121]
	s_add_u32 s66, s66, s67
	v_mfma_f32_16x16x32_bf16 v[30:33], v[178:181], v[154:157], v[30:33]
	s_add_u32 s66, s14, s66
	v_mfma_f32_16x16x32_bf16 v[46:49], v[182:185], v[146:149], v[46:49]
	s_addc_u32 s67, s15, 0
	v_mfma_f32_16x16x32_bf16 v[14:17], v[182:185], v[154:157], v[14:17]
	v_mfma_f32_16x16x32_bf16 v[82:85], v[170:173], v[150:153], v[82:85]
	v_mfma_f32_16x16x32_bf16 v[22:25], v[170:173], v[158:161], v[22:25]
	v_mfma_f32_16x16x32_bf16 v[34:37], v[174:177], v[150:153], v[34:37]
	v_mfma_f32_16x16x32_bf16 v[6:9], v[174:177], v[158:161], v[6:9]
	v_mfma_f32_16x16x32_bf16 v[118:121], v[186:189], v[150:153], v[118:121]
	v_mfma_f32_16x16x32_bf16 v[30:33], v[186:189], v[158:161], v[30:33]
	v_mfma_f32_16x16x32_bf16 v[46:49], v[190:193], v[150:153], v[46:49]
	v_mfma_f32_16x16x32_bf16 v[14:17], v[190:193], v[158:161], v[14:17]
	s_setprio 0
	s_barrier
.LBB3_11:
	v_add_u32_e32 v172, s43, v207
	v_pk_fma_f32 v[244:245], v[244:245], -0.5, -0.5 op_sel_hi:[1,0,0]
	v_pk_fma_f32 v[246:247], v[246:247], -0.5, -0.5 op_sel_hi:[1,0,0]
	v_pk_fma_f32 v[248:249], v[248:249], -0.5, -0.5 op_sel_hi:[1,0,0]
	v_pk_fma_f32 v[250:251], v[250:251], -0.5, -0.5 op_sel_hi:[1,0,0]
	v_pk_fma_f32 v[252:253], v[252:253], -0.5, -0.5 op_sel_hi:[1,0,0]
	v_pk_fma_f32 v[254:255], v[254:255], -0.5, -0.5 op_sel_hi:[1,0,0]
	v_pk_fma_f32 v[232:233], v[232:233], -0.5, -0.5 op_sel_hi:[1,0,0]
	v_pk_fma_f32 v[234:235], v[234:235], -0.5, -0.5 op_sel_hi:[1,0,0]
	v_pk_mul_f32 v[134:135], v[244:245], v[246:247]
	v_pk_mul_f32 v[146:147], v[248:249], v[250:251]
	v_pk_mul_f32 v[180:181], v[252:253], v[254:255]
	v_pk_mul_f32 v[236:237], v[232:233], v[234:235]
	v_mul_f32_e32 v188, v134, v135
	v_mul_f32_e32 v190, v146, v147
	v_mul_f32_e32 v189, v180, v181
	v_mul_f32_e32 v191, v236, v237
	v_pk_mul_f32 v[192:193], v[188:189], v[190:191]
	v_mul_f32_e32 v162, v192, v193
	v_rcp_f32_e32 v173, v162
	v_pk_add_f32 v[164:165], v[114:115], v[116:117]
	v_pk_add_f32 v[164:165], v[164:165], v[78:79]
	v_pk_add_f32 v[164:165], v[164:165], v[80:81]
	v_pk_add_f32 v[164:165], v[164:165], v[106:107]
	v_pk_add_f32 v[164:165], v[164:165], v[108:109]
	v_pk_add_f32 v[164:165], v[164:165], v[70:71]
	v_pk_add_f32 v[164:165], v[164:165], v[72:73]
	v_pk_mul_f32 v[230:231], v[172:173], v[192:193] op_sel:[1,1] op_sel_hi:[1,0]
	v_pk_mul_f32 v[192:193], v[230:231], v[190:191]
	v_pk_mul_f32 v[190:191], v[230:231], v[188:189]
	v_pk_mul_f32 v[136:137], v[192:193], v[134:135] op_sel:[0,1] op_sel_hi:[0,0]
	v_pk_mul_f32 v[148:149], v[190:191], v[146:147] op_sel:[0,1] op_sel_hi:[0,0]
	v_pk_mul_f32 v[182:183], v[192:193], v[180:181] op_sel:[1,1] op_sel_hi:[1,0]
	v_pk_mul_f32 v[238:239], v[190:191], v[236:237] op_sel:[1,1] op_sel_hi:[1,0]
	v_pk_fma_f32 v[138:139], v[136:137], v[246:247], 1.0 op_sel_hi:[1,1,0]
	v_pk_fma_f32 v[140:141], v[136:137], v[244:245], 1.0 op_sel_hi:[1,1,0]
	v_pk_fma_f32 v[150:151], v[148:149], v[250:251], 1.0 op_sel_hi:[1,1,0]
	v_pk_fma_f32 v[152:153], v[148:149], v[248:249], 1.0 op_sel_hi:[1,1,0]
	v_pk_fma_f32 v[184:185], v[182:183], v[254:255], 1.0 op_sel_hi:[1,1,0]
	v_pk_fma_f32 v[186:187], v[182:183], v[252:253], 1.0 op_sel_hi:[1,1,0]
	v_pk_fma_f32 v[240:241], v[238:239], v[234:235], 1.0 op_sel_hi:[1,1,0]
	v_pk_fma_f32 v[242:243], v[238:239], v[232:233], 1.0 op_sel_hi:[1,1,0]
	v_cvt_pk_bf16_f32 v154, v138, v139
	v_cvt_pk_bf16_f32 v155, v140, v141
	v_cvt_pk_bf16_f32 v156, v150, v151
	v_cvt_pk_bf16_f32 v157, v152, v153
	v_cvt_pk_bf16_f32 v158, v184, v185
	v_cvt_pk_bf16_f32 v159, v186, v187
	v_cvt_pk_bf16_f32 v160, v240, v241
	v_cvt_pk_bf16_f32 v161, v242, v243
	ds_read_b128 v[114:117], v172
	ds_read_b128 v[78:81], v172 offset:64
	ds_read_b128 v[106:109], v172 offset:128
	ds_read_b128 v[70:73], v172 offset:192
	v_permlane16_swap_b32_e32 v154, v156
	v_permlane16_swap_b32_e32 v155, v157
	global_store_dwordx4 v228, v[154:157], s[58:59] nt
	s_bitcmp1_b32 s20, 12
	s_cbranch_scc1 .Lg1_noX
	s_barrier
